# out-projection GEMM epilogue: residual rows of the next chunk are prefetched one chunk ahead into spare registers, products computed in place, and each chunk's wait counts only its own loads (the four
# speedup vs baseline: 1.0062x; 1.0035x over previous
;     __device__ __forceinline__ float* mods() const { return (float*)(ws + WS_MODS); }
;     __device__ __forceinline__ void operator()(const AccT& acc, const gm::GUnit& u, int wr, int wc, int fr, int fq) const {
;         asm volatile("" : "+v"(fr), "+v"(fq));
;         const bool lat = u.pm < 256;
;         const int b = lat ? (u.pm >> 5) : 8;
;         const float* gp = mods + (size_t)b * 6144 + 2 * 1024 + u.pn * 256 + wc * 32 + 4 * fq;
;         f32x4 gv[2][2];
; #pragma unroll
;         for (int bj = 0; bj < 2; ++bj)
; #pragma unroll
;             for (int n = 0; n < 2; ++n) gv[bj][n] = *(const f32x4*)(gp + bj * 128 + n * 16);
; #pragma unroll
;         for (int q = 0; q < 4; ++q) {
;             const int ai = q >> 1, m0 = (q & 1) * 2;
;             f32x4 xv[2][2][2];
; #pragma unroll
;             for (int mi = 0; mi < 2; ++mi) {
;                 const int row = u.pm * 256 + ai * 128 + wr * 64 + (m0 + mi) * 16 + fr;
;                 const float* ip = xin + (size_t)row * DM + u.pn * 256 + wc * 32 + 4 * fq + (lat ? 0ll : din);
; #pragma unroll
;                 for (int bj = 0; bj < 2; ++bj)
; #pragma unroll
;                     for (int n = 0; n < 2; ++n) xv[mi][bj][n] = *(const f32x4*)(ip + bj * 128 + n * 16);
;             }
;             __builtin_amdgcn_sched_barrier(0);
; #pragma unroll
;             for (int mi = 0; mi < 2; ++mi) {
;                 const int m = m0 + mi, row = u.pm * 256 + ai * 128 + wr * 64 + m * 16 + fr;
;                 float* op = xout + (size_t)row * DM + u.pn * 256 + wc * 32 + 4 * fq + (lat ? 0ll : dout);
; #pragma unroll
;                 for (int bj = 0; bj < 2; ++bj)
; #pragma unroll
;                     for (int n = 0; n < 2; ++n) *(f32x4*)(op + bj * 128 + n * 16) = xv[mi][bj][n] + gv[bj][n] * acc[ai][bj][m][n];
;             }
;             __builtin_amdgcn_sched_barrier(0);
;         }
;     }
.LBB0_814:
	s_lshl_b64 s[8:9], s[8:9], 2
	s_add_u32 s24, s62, s8
	s_addc_u32 s25, s63, s9
	s_lshl_b32 s8, s54, 8
	s_ashr_i32 s9, s8, 31
	s_lshl_b64 s[8:9], s[8:9], 2
	s_add_u32 s24, s24, s8
	s_addc_u32 s25, s25, s9
	v_lshlrev_b32_e32 v130, 2, v130
	s_add_u32 s24, s24, s76
	v_ashrrev_i32_e32 v131, 31, v130
	s_addc_u32 s25, s25, 0
	v_lshlrev_b64 v[148:149], 2, v[130:131]
	v_lshl_add_u64 v[130:131], s[24:25], 0, v[148:149]
	s_mov_b64 s[24:25], 0x2000
	v_lshl_add_u64 v[132:133], v[130:131], 0, s[24:25]
	s_movk_i32 s24, 0x2000
	v_add_co_u32_e32 v130, vcc, s24, v130
	s_lshl_b32 s24, s52, 8
	s_add_i32 s24, s24, s71
	v_add_u32_e32 v150, s24, v150
	s_add_u32 s24, s74, s8
	s_addc_u32 s25, s75, s9
	v_add_u32_e32 v170, 16, v150
	v_lshl_add_u64 v[152:153], s[24:25], 0, v[148:149]
	v_ashrrev_i32_e32 v151, 31, v150
	v_ashrrev_i32_e32 v171, 31, v170
	v_lshl_add_u64 v[152:153], s[22:23], 2, v[152:153]
	v_lshlrev_b64 v[178:179], 12, v[150:151]
	v_lshlrev_b64 v[200:201], 12, v[170:171]
	v_addc_co_u32_e32 v131, vcc, 0, v131, vcc
	v_lshl_add_u64 v[166:167], v[152:153], 0, v[178:179]
	v_lshl_add_u64 v[192:193], v[152:153], 0, v[200:201]
	global_load_dwordx4 v[138:141], v[132:133], off offset:64
	global_load_dwordx4 v[134:137], v[132:133], off offset:512
	global_load_dwordx4 v[142:145], v[130:131], off
	s_nop 0
	global_load_dwordx4 v[130:133], v[132:133], off offset:576
	s_nop 0
	global_load_dwordx4 v[154:157], v[166:167], off
	global_load_dwordx4 v[158:161], v[166:167], off offset:64
	global_load_dwordx4 v[162:165], v[166:167], off offset:512
	s_nop 0
	global_load_dwordx4 v[166:169], v[166:167], off offset:576
	s_nop 0
	global_load_dwordx4 v[170:173], v[192:193], off
	global_load_dwordx4 v[174:177], v[192:193], off offset:64
	global_load_dwordx4 v[188:191], v[192:193], off offset:512
	s_nop 0
	global_load_dwordx4 v[192:195], v[192:193], off offset:576
	v_lshl_add_u64 v[200:201], v[152:153], 0, v[178:179]
	v_add_co_u32_e32 v214, vcc, 0x20000, v200
	v_addc_co_u32_e32 v215, vcc, 0, v201, vcc
	global_load_dwordx4 v[202:205], v[214:215], off
	global_load_dwordx4 v[206:209], v[214:215], off offset:64
	global_load_dwordx4 v[210:213], v[214:215], off offset:512
	global_load_dwordx4 v[214:217], v[214:215], off offset:576
	v_add_co_u32_e32 v246, vcc, 0x30000, v200
	v_addc_co_u32_e32 v247, vcc, 0, v201, vcc
	global_load_dwordx2 v[218:219], v[246:247], off
	global_load_dwordx2 v[234:235], v[246:247], off offset:8
	global_load_dwordx4 v[238:241], v[246:247], off offset:64
	global_load_dwordx4 v[242:245], v[246:247], off offset:512
	global_load_dwordx4 v[246:249], v[246:247], off offset:576
	v_lshl_add_u64 v[178:179], s[36:37], 0, v[178:179]
	v_lshl_add_u64 v[178:179], v[178:179], 0, s[8:9]
	v_lshl_add_u64 v[178:179], v[178:179], 0, s[76:77]
	v_lshl_add_u64 v[178:179], v[178:179], 0, v[148:149]
	s_lshl_b64 s[18:19], s[18:19], 2
	v_lshl_add_u64 v[178:179], v[178:179], 0, s[18:19]
	s_waitcnt vmcnt(9)
	v_pk_fma_f32 v[106:107], v[106:107], v[130:131], v[166:167]
	v_pk_fma_f32 v[108:109], v[108:109], v[132:133], v[168:169]
	v_pk_fma_f32 v[114:115], v[114:115], v[134:135], v[162:163]
	v_pk_fma_f32 v[116:117], v[116:117], v[136:137], v[164:165]
	v_pk_fma_f32 v[126:127], v[126:127], v[142:143], v[154:155]
	v_pk_fma_f32 v[128:129], v[128:129], v[144:145], v[156:157]
	v_pk_fma_f32 v[122:123], v[122:123], v[138:139], v[158:159]
	v_pk_fma_f32 v[124:125], v[124:125], v[140:141], v[160:161]
	v_pk_fma_f32 v[98:99], v[98:99], v[130:131], v[192:193]
	v_pk_fma_f32 v[100:101], v[100:101], v[132:133], v[194:195]
	v_pk_fma_f32 v[102:103], v[102:103], v[134:135], v[188:189]
	v_pk_fma_f32 v[104:105], v[104:105], v[136:137], v[190:191]
	v_pk_fma_f32 v[118:119], v[118:119], v[142:143], v[170:171]
	v_pk_fma_f32 v[120:121], v[120:121], v[144:145], v[172:173]
	v_pk_fma_f32 v[110:111], v[110:111], v[138:139], v[174:175]
	v_pk_fma_f32 v[112:113], v[112:113], v[140:141], v[176:177]
	v_mov_b32_e32 v154, v178
	v_mov_b32_e32 v155, v179
	v_add_co_u32_e32 v158, vcc, 0x10000, v178
	v_addc_co_u32_e32 v159, vcc, 0, v179, vcc
	s_nop 0
	global_store_dwordx4 v[154:155], v[126:129], off
	global_store_dwordx4 v[154:155], v[122:125], off offset:64
	global_store_dwordx4 v[154:155], v[114:117], off offset:512
	global_store_dwordx4 v[154:155], v[106:109], off offset:576
	global_store_dwordx4 v[158:159], v[118:121], off
	global_store_dwordx4 v[158:159], v[110:113], off offset:64
	global_store_dwordx4 v[158:159], v[102:105], off offset:512
	global_store_dwordx4 v[158:159], v[98:101], off offset:576
	v_add_co_u32_e32 v166, vcc, 0x80000, v200
	v_addc_co_u32_e32 v167, vcc, 0, v201, vcc
	global_load_dwordx4 v[154:157], v[166:167], off
	global_load_dwordx4 v[158:161], v[166:167], off offset:64
	global_load_dwordx4 v[162:165], v[166:167], off offset:512
	global_load_dwordx4 v[166:169], v[166:167], off offset:576
	v_add_co_u32_e32 v192, vcc, 0x90000, v200
	v_addc_co_u32_e32 v193, vcc, 0, v201, vcc
	global_load_dwordx4 v[170:173], v[192:193], off
	global_load_dwordx4 v[174:177], v[192:193], off offset:64
	global_load_dwordx4 v[188:191], v[192:193], off offset:512
	global_load_dwordx4 v[192:195], v[192:193], off offset:576
	s_waitcnt vmcnt(16)
;     __device__ __forceinline__ void operator()(const AccT& acc, const gm::GUnit& u, int wr, int wc, int fr, int fq) const {
;     ...
;         for (int q = 0; q < 4; ++q) {
;             const int ai = q >> 1, m0 = (q & 1) * 2;
;             f32x4 xv[2][2][2];
; #pragma unroll
;             for (int mi = 0; mi < 2; ++mi) {
;                 const int row = u.pm * 256 + ai * 128 + wr * 64 + (m0 + mi) * 16 + fr;
;                 const float* ip = xin + (size_t)row * DM + u.pn * 256 + wc * 32 + 4 * fq + (lat ? 0ll : din);
; #pragma unroll
;                 for (int bj = 0; bj < 2; ++bj)
; #pragma unroll
;                     for (int n = 0; n < 2; ++n) xv[mi][bj][n] = *(const f32x4*)(ip + bj * 128 + n * 16);
;             }
;             __builtin_amdgcn_sched_barrier(0);
; #pragma unroll
;             for (int mi = 0; mi < 2; ++mi) {
;                 const int m = m0 + mi, row = u.pm * 256 + ai * 128 + wr * 64 + m * 16 + fr;
;                 float* op = xout + (size_t)row * DM + u.pn * 256 + wc * 32 + 4 * fq + (lat ? 0ll : dout);
; #pragma unroll
;                 for (int bj = 0; bj < 2; ++bj)
; #pragma unroll
;                     for (int n = 0; n < 2; ++n) *(f32x4*)(op + bj * 128 + n * 16) = xv[mi][bj][n] + gv[bj][n] * acc[ai][bj][m][n];
;             }
;             __builtin_amdgcn_sched_barrier(0);
;         }
;     }
	v_pk_fma_f32 v[74:75], v[74:75], v[130:131], v[214:215]
	v_pk_fma_f32 v[76:77], v[76:77], v[132:133], v[216:217]
	v_pk_fma_f32 v[82:83], v[82:83], v[134:135], v[210:211]
	v_pk_fma_f32 v[84:85], v[84:85], v[136:137], v[212:213]
	v_pk_fma_f32 v[94:95], v[94:95], v[142:143], v[202:203]
	v_pk_fma_f32 v[96:97], v[96:97], v[144:145], v[204:205]
	v_pk_fma_f32 v[90:91], v[90:91], v[138:139], v[206:207]
	v_pk_fma_f32 v[92:93], v[92:93], v[140:141], v[208:209]
	v_pk_fma_f32 v[66:67], v[66:67], v[130:131], v[246:247]
	v_pk_fma_f32 v[68:69], v[68:69], v[132:133], v[248:249]
	v_pk_fma_f32 v[70:71], v[70:71], v[134:135], v[242:243]
	v_pk_fma_f32 v[72:73], v[72:73], v[136:137], v[244:245]
	v_pk_fma_f32 v[86:87], v[86:87], v[142:143], v[218:219]
	v_pk_fma_f32 v[88:89], v[88:89], v[144:145], v[234:235]
	v_pk_fma_f32 v[78:79], v[78:79], v[138:139], v[238:239]
	v_pk_fma_f32 v[80:81], v[80:81], v[140:141], v[240:241]
	v_add_co_u32_e32 v202, vcc, 0x20000, v178
	v_addc_co_u32_e32 v203, vcc, 0, v179, vcc
	v_add_co_u32_e32 v206, vcc, 0x30000, v178
	v_addc_co_u32_e32 v207, vcc, 0, v179, vcc
	s_nop 0
	global_store_dwordx4 v[202:203], v[94:97], off
	global_store_dwordx4 v[202:203], v[90:93], off offset:64
	global_store_dwordx4 v[202:203], v[82:85], off offset:512
	global_store_dwordx4 v[202:203], v[74:77], off offset:576
	global_store_dwordx4 v[206:207], v[86:89], off
	global_store_dwordx4 v[206:207], v[78:81], off offset:64
	global_store_dwordx4 v[206:207], v[70:73], off offset:512
	global_store_dwordx4 v[206:207], v[66:69], off offset:576
	v_add_co_u32_e32 v214, vcc, 0xa0000, v200
	v_addc_co_u32_e32 v215, vcc, 0, v201, vcc
	global_load_dwordx4 v[202:205], v[214:215], off
	global_load_dwordx4 v[206:209], v[214:215], off offset:64
	global_load_dwordx4 v[210:213], v[214:215], off offset:512
	global_load_dwordx4 v[214:217], v[214:215], off offset:576
	v_add_co_u32_e32 v246, vcc, 0xb0000, v200
	v_addc_co_u32_e32 v247, vcc, 0, v201, vcc
	global_load_dwordx2 v[218:219], v[246:247], off
	global_load_dwordx2 v[234:235], v[246:247], off offset:8
	global_load_dwordx4 v[238:241], v[246:247], off offset:64
	global_load_dwordx4 v[242:245], v[246:247], off offset:512
	global_load_dwordx4 v[246:249], v[246:247], off offset:576
	s_waitcnt vmcnt(17)
	v_pk_fma_f32 v[46:47], v[46:47], v[130:131], v[166:167]
	v_pk_fma_f32 v[48:49], v[48:49], v[132:133], v[168:169]
	v_pk_fma_f32 v[54:55], v[54:55], v[134:135], v[162:163]
	v_pk_fma_f32 v[56:57], v[56:57], v[136:137], v[164:165]
	v_pk_fma_f32 v[62:63], v[62:63], v[142:143], v[154:155]
	v_pk_fma_f32 v[64:65], v[64:65], v[144:145], v[156:157]
	v_pk_fma_f32 v[58:59], v[58:59], v[138:139], v[158:159]
	v_pk_fma_f32 v[60:61], v[60:61], v[140:141], v[160:161]
	v_pk_fma_f32 v[34:35], v[34:35], v[130:131], v[192:193]
	v_pk_fma_f32 v[36:37], v[36:37], v[132:133], v[194:195]
	v_pk_fma_f32 v[38:39], v[38:39], v[134:135], v[188:189]
	v_pk_fma_f32 v[40:41], v[40:41], v[136:137], v[190:191]
	v_pk_fma_f32 v[50:51], v[50:51], v[142:143], v[170:171]
	v_pk_fma_f32 v[52:53], v[52:53], v[144:145], v[172:173]
	v_pk_fma_f32 v[42:43], v[42:43], v[138:139], v[174:175]
	v_pk_fma_f32 v[44:45], v[44:45], v[140:141], v[176:177]
	v_add_co_u32_e32 v154, vcc, 0x80000, v178
	v_addc_co_u32_e32 v155, vcc, 0, v179, vcc
	v_add_co_u32_e32 v158, vcc, 0x90000, v178
	v_addc_co_u32_e32 v159, vcc, 0, v179, vcc
	s_nop 0
	global_store_dwordx4 v[154:155], v[62:65], off
	global_store_dwordx4 v[154:155], v[58:61], off offset:64
	global_store_dwordx4 v[154:155], v[54:57], off offset:512
	global_store_dwordx4 v[154:155], v[46:49], off offset:576
	global_store_dwordx4 v[158:159], v[50:53], off
	global_store_dwordx4 v[158:159], v[42:45], off offset:64
	global_store_dwordx4 v[158:159], v[38:41], off offset:512
	global_store_dwordx4 v[158:159], v[34:37], off offset:576
	s_waitcnt vmcnt(8)
	v_pk_fma_f32 v[14:15], v[14:15], v[130:131], v[214:215]
	v_pk_fma_f32 v[16:17], v[16:17], v[132:133], v[216:217]
	v_pk_fma_f32 v[22:23], v[22:23], v[134:135], v[210:211]
	v_pk_fma_f32 v[24:25], v[24:25], v[136:137], v[212:213]
	v_pk_fma_f32 v[30:31], v[30:31], v[142:143], v[202:203]
	v_pk_fma_f32 v[32:33], v[32:33], v[144:145], v[204:205]
	v_pk_fma_f32 v[26:27], v[26:27], v[138:139], v[206:207]
	v_pk_fma_f32 v[28:29], v[28:29], v[140:141], v[208:209]
	v_pk_fma_f32 v[2:3], v[2:3], v[130:131], v[246:247]
	v_pk_fma_f32 v[4:5], v[4:5], v[132:133], v[248:249]
	v_pk_fma_f32 v[6:7], v[6:7], v[134:135], v[242:243]
	v_pk_fma_f32 v[8:9], v[8:9], v[136:137], v[244:245]
	v_pk_fma_f32 v[18:19], v[18:19], v[142:143], v[218:219]
	v_pk_fma_f32 v[20:21], v[20:21], v[144:145], v[234:235]
	v_pk_fma_f32 v[10:11], v[10:11], v[138:139], v[238:239]
	v_pk_fma_f32 v[12:13], v[12:13], v[140:141], v[240:241]
	v_add_co_u32_e32 v202, vcc, 0xa0000, v178
	v_addc_co_u32_e32 v203, vcc, 0, v179, vcc
	v_add_co_u32_e32 v206, vcc, 0xb0000, v178
	v_addc_co_u32_e32 v207, vcc, 0, v179, vcc
	s_nop 0
	global_store_dwordx4 v[202:203], v[30:33], off
	global_store_dwordx4 v[202:203], v[26:29], off offset:64
	global_store_dwordx4 v[202:203], v[22:25], off offset:512
	global_store_dwordx4 v[202:203], v[14:17], off offset:576
	global_store_dwordx4 v[206:207], v[18:21], off
	global_store_dwordx4 v[206:207], v[10:13], off offset:64
	global_store_dwordx4 v[206:207], v[6:9], off offset:512
	global_store_dwordx4 v[206:207], v[2:5], off offset:576
	s_and_b64 vcc, exec, s[58:59]
	s_mov_b32 s52, s46
	s_mov_b32 s54, s42
	s_mov_b64 s[8:9], s[48:49]
	s_mov_b64 s[18:19], s[50:51]
	s_mov_b32 s43, s80
	s_cbranch_vccnz .LBB0_840
